# P9+P10 epilogues: bias folded into accumulator init, up-branch and down GEMM power-of-two factors moved into the MFMA block scale, packed f32 math, permlane16_swap paired 16-byte stores
# speedup vs baseline: 1.0153x; 1.0015x over previous
.LBB0_1412:
	s_lshl_b32 s4, s4, 5
	s_and_b32 s12, s4, 0x60
	s_lshl_b32 s4, s12, 2
	s_add_i32 s14, s4, 0
	s_mov_b64 s[4:5], 0x80
	s_add_i32 s40, s29, 0x18000
	v_lshl_add_u64 v[6:7], v[6:7], 0, s[4:5]
	s_mov_b32 m0, s40
	s_add_i32 s41, s29, 0x1a000
	s_lshl_b32 s9, s8, 13
	s_lshl_b32 s13, s12, 7
	s_waitcnt vmcnt(4)
	s_barrier
	global_load_lds_dwordx4 v[6:7], off
	v_lshl_add_u64 v[4:5], v[4:5], 0, s[4:5]
	s_mov_b32 m0, s41
	s_add_i32 s42, s29, 0x8000
	s_add_i32 s43, s29, 0xa000
	global_load_lds_dwordx4 v[4:5], off
	v_lshl_add_u64 v[2:3], v[2:3], 0, s[4:5]
	s_mov_b32 m0, s42
	s_add_u32 s10, s20, 0x40080
	global_load_lds_dwordx4 v[2:3], off
	v_lshl_add_u64 v[0:1], v[0:1], 0, s[4:5]
	s_mov_b32 m0, s43
	s_addc_u32 s11, s21, 0
	s_add_i32 s44, s29, 0x1c000
	global_load_lds_dwordx4 v[0:1], off
	v_lshl_add_u64 v[0:1], s[10:11], 0, v[146:147]
	s_mov_b32 m0, s44
	s_add_i32 s45, s29, 0x1e000
	global_load_lds_dwordx4 v[0:1], off
	v_lshl_add_u64 v[0:1], s[10:11], 0, v[144:145]
	s_mov_b32 m0, s45
	v_lshlrev_b32_e32 v4, 2, v8
	global_load_lds_dwordx4 v[0:1], off
	v_lshrrev_b32_e32 v0, 1, v8
	v_and_b32_e32 v1, 15, v8
	v_and_b32_e32 v2, 24, v0
	v_lshlrev_b32_e32 v3, 1, v2
	v_lshl_or_b32 v0, s8, 6, v1
	v_lshlrev_b32_e32 v1, 6, v1
	v_and_b32_e32 v4, 32, v4
	v_bitop3_b32 v1, v1, v4, v3 bitop3:0x36
	s_add_i32 s13, s13, 0
	v_add_u32_e32 v3, s13, v1
	v_add_u32_e32 v4, 0, v1
	v_ashrrev_i32_e32 v1, 31, v0
	v_lshlrev_b64 v[0:1], 11, v[0:1]
	v_lshl_add_u64 v[0:1], s[6:7], 0, v[0:1]
	s_mov_b64 s[6:7], 0x4b300000
	v_lshl_add_u64 v[156:157], v[0:1], 0, s[6:7]
	v_lshlrev_b32_e32 v0, 14, v9
	v_and_b32_e32 v0, 0xffff8000, v0
	v_lshl_add_u32 v0, v10, 11, v0
	v_and_b32_e32 v1, 1, v9
	v_lshl_or_b32 v0, v1, 6, v0
	v_lshlrev_b32_e32 v1, 1, v11
	v_add3_u32 v158, v0, v1, s38
	v_lshlrev_b32_e32 v0, 14, v13
	v_and_b32_e32 v0, 0xffff8000, v0
	s_waitcnt vmcnt(6)
	v_lshl_add_u32 v0, v12, 11, v0
	v_and_b32_e32 v1, 1, v13
	s_add_i32 s14, s14, 0x22a00
	v_lshl_or_b32 v0, v1, 6, v0
	v_lshlrev_b32_e32 v1, 1, v14
	v_mov_b32_e32 v153, v147
	v_mov_b32_e32 v155, v147
	s_mov_b32 s46, 0x18000
	s_mov_b32 s47, 0x8000
	v_add_u32_e32 v170, 0x10000, v3
	v_add_u32_e32 v171, 0x14000, v3
	v_add_u32_e32 v172, 0x18000, v3
	v_add_u32_e32 v173, 0x1c000, v3
	v_lshl_add_u32 v174, v2, 2, s14
	v_add_u32_e32 v175, 0x10400, v3
	v_add_u32_e32 v176, 0x10800, v3
	v_add_u32_e32 v177, 0x10c00, v3
	v_add_u32_e32 v178, 0x14400, v3
	v_add_u32_e32 v179, 0x14800, v3
	v_add_u32_e32 v180, 0x14c00, v3
	v_add_u32_e32 v181, 0x18400, v3
	v_add_u32_e32 v182, 0x18800, v3
	v_add_u32_e32 v183, 0x18c00, v3
	v_add_u32_e32 v184, 0x1c400, v3
	v_add_u32_e32 v185, 0x1c800, v3
	v_add_u32_e32 v186, 0x1cc00, v3
	v_or_b32_e32 v187, s12, v2
	v_mov_b32_e32 v159, v147
	v_add3_u32 v160, v0, v1, s38
	v_mov_b32_e32 v161, v147
	v_add_u32_e32 v188, s9, v4
	v_mov_b32_e32 v189, 0x7d7d7d7d
	s_mov_b64 s[62:63], 0x10000
	s_mov_b32 s64, 0x30000
	s_mov_b32 s65, 0
	v_mov_b32_e32 v190, 0x7d7d7d7d
	s_mov_b32 s6, 0x41800000
	s_mov_b32 s7, 0xc3e00000
	s_mov_b32 s48, 0x48000
	s_mov_b32 s49, 0x50000
	s_mov_b32 s50, 0x58000
	v_mov_b32_e32 v191, 0x43e00000
	s_mov_b32 s51, 0
	s_barrier

.LBB0_1418:
	s_ashr_i32 s9, s8, 31
	s_lshl_b64 s[14:15], s[8:9], 19
	s_add_u32 s14, s25, s14
	s_addc_u32 s15, s26, s15
	s_and_b64 s[22:23], s[22:23], exec
	s_cselect_b32 s9, s15, s19
	s_cselect_b32 s55, s14, s18
	s_add_u32 s18, s18, 0x80
	s_addc_u32 s19, s19, 0
	s_add_u32 s56, s20, 0x100
	s_addc_u32 s57, s21, 0
	s_mov_b32 s58, -2
	v_lshl_add_u32 v208, s17, 10, v174
	ds_read_b128 v[192:195], v208
	ds_read_b128 v[196:199], v208 offset:16
	ds_read_b128 v[200:203], v208 offset:512
	ds_read_b128 v[204:207], v208 offset:528
	s_mov_b32 s59, 0x41800000
	s_waitcnt lgkmcnt(0)
	v_mul_f32_e32 v192, s59, v192
	v_mul_f32_e32 v193, s59, v193
	v_mul_f32_e32 v194, s59, v194
	v_mul_f32_e32 v195, s59, v195
	v_mul_f32_e32 v196, s59, v196
	v_mul_f32_e32 v197, s59, v197
	v_mul_f32_e32 v198, s59, v198
	v_mul_f32_e32 v199, s59, v199
	v_mul_f32_e32 v200, s59, v200
	v_mul_f32_e32 v201, s59, v201
	v_mul_f32_e32 v202, s59, v202
	v_mul_f32_e32 v203, s59, v203
	v_mul_f32_e32 v204, s59, v204
	v_mul_f32_e32 v205, s59, v205
	v_mul_f32_e32 v206, s59, v206
	v_mul_f32_e32 v207, s59, v207
	v_mov_b32_e32 v140, v192
	v_mov_b32_e32 v141, v193
	v_mov_b32_e32 v142, v194
	v_mov_b32_e32 v143, v195
	v_mov_b32_e32 v136, v196
	v_mov_b32_e32 v137, v197
	v_mov_b32_e32 v138, v198
	v_mov_b32_e32 v139, v199
	v_mov_b32_e32 v132, v192
	v_mov_b32_e32 v133, v193
	v_mov_b32_e32 v134, v194
	v_mov_b32_e32 v135, v195
	v_mov_b32_e32 v128, v196
	v_mov_b32_e32 v129, v197
	v_mov_b32_e32 v130, v198
	v_mov_b32_e32 v131, v199
	v_mov_b32_e32 v124, v192
	v_mov_b32_e32 v125, v193
	v_mov_b32_e32 v126, v194
	v_mov_b32_e32 v127, v195
	v_mov_b32_e32 v120, v196
	v_mov_b32_e32 v121, v197
	v_mov_b32_e32 v122, v198
	v_mov_b32_e32 v123, v199
	v_mov_b32_e32 v116, v192
	v_mov_b32_e32 v117, v193
	v_mov_b32_e32 v118, v194
	v_mov_b32_e32 v119, v195
	v_mov_b32_e32 v112, v196
	v_mov_b32_e32 v113, v197
	v_mov_b32_e32 v114, v198
	v_mov_b32_e32 v115, v199
	v_mov_b32_e32 v84, v200
	v_mov_b32_e32 v85, v201
	v_mov_b32_e32 v86, v202
	v_mov_b32_e32 v87, v203
	v_mov_b32_e32 v76, v204
	v_mov_b32_e32 v77, v205
	v_mov_b32_e32 v78, v206
	v_mov_b32_e32 v79, v207
	v_mov_b32_e32 v68, v200
	v_mov_b32_e32 v69, v201
	v_mov_b32_e32 v70, v202
	v_mov_b32_e32 v71, v203
	v_mov_b32_e32 v64, v204
	v_mov_b32_e32 v65, v205
	v_mov_b32_e32 v66, v206
	v_mov_b32_e32 v67, v207
	v_mov_b32_e32 v60, v200
	v_mov_b32_e32 v61, v201
	v_mov_b32_e32 v62, v202
	v_mov_b32_e32 v63, v203
	v_mov_b32_e32 v56, v204
	v_mov_b32_e32 v57, v205
	v_mov_b32_e32 v58, v206
	v_mov_b32_e32 v59, v207
	v_mov_b32_e32 v52, v200
	v_mov_b32_e32 v53, v201
	v_mov_b32_e32 v54, v202
	v_mov_b32_e32 v55, v203
	v_mov_b32_e32 v48, v204
	v_mov_b32_e32 v49, v205
	v_mov_b32_e32 v50, v206
	v_mov_b32_e32 v51, v207
	v_mov_b32_e32 v108, v192
	v_mov_b32_e32 v109, v193
	v_mov_b32_e32 v110, v194
	v_mov_b32_e32 v111, v195
	v_mov_b32_e32 v104, v196
	v_mov_b32_e32 v105, v197
	v_mov_b32_e32 v106, v198
	v_mov_b32_e32 v107, v199
	v_mov_b32_e32 v100, v192
	v_mov_b32_e32 v101, v193
	v_mov_b32_e32 v102, v194
	v_mov_b32_e32 v103, v195
	v_mov_b32_e32 v96, v196
	v_mov_b32_e32 v97, v197
	v_mov_b32_e32 v98, v198
	v_mov_b32_e32 v99, v199
	v_mov_b32_e32 v92, v192
	v_mov_b32_e32 v93, v193
	v_mov_b32_e32 v94, v194
	v_mov_b32_e32 v95, v195
	v_mov_b32_e32 v88, v196
	v_mov_b32_e32 v89, v197
	v_mov_b32_e32 v90, v198
	v_mov_b32_e32 v91, v199
	v_mov_b32_e32 v80, v192
	v_mov_b32_e32 v81, v193
	v_mov_b32_e32 v82, v194
	v_mov_b32_e32 v83, v195
	v_mov_b32_e32 v72, v196
	v_mov_b32_e32 v73, v197
	v_mov_b32_e32 v74, v198
	v_mov_b32_e32 v75, v199
	v_mov_b32_e32 v44, v200
	v_mov_b32_e32 v45, v201
	v_mov_b32_e32 v46, v202
	v_mov_b32_e32 v47, v203
	v_mov_b32_e32 v40, v204
	v_mov_b32_e32 v41, v205
	v_mov_b32_e32 v42, v206
	v_mov_b32_e32 v43, v207
	v_mov_b32_e32 v36, v200
	v_mov_b32_e32 v37, v201
	v_mov_b32_e32 v38, v202
	v_mov_b32_e32 v39, v203
	v_mov_b32_e32 v32, v204
	v_mov_b32_e32 v33, v205
	v_mov_b32_e32 v34, v206
	v_mov_b32_e32 v35, v207
	v_mov_b32_e32 v28, v200
	v_mov_b32_e32 v29, v201
	v_mov_b32_e32 v30, v202
	v_mov_b32_e32 v31, v203
	v_mov_b32_e32 v24, v204
	v_mov_b32_e32 v25, v205
	v_mov_b32_e32 v26, v206
	v_mov_b32_e32 v27, v207
	v_mov_b32_e32 v20, v200
	v_mov_b32_e32 v21, v201
	v_mov_b32_e32 v22, v202
	v_mov_b32_e32 v23, v203
	v_mov_b32_e32 v16, v204
	v_mov_b32_e32 v17, v205
	v_mov_b32_e32 v18, v206
	v_mov_b32_e32 v19, v207
.LBB0_1419:
	ds_read_b128 v[0:3], v170
	ds_read_b128 v[4:7], v175
	ds_read_b128 v[8:11], v176
	ds_read_b128 v[12:15], v177
	s_add_u32 s20, s18, 0x80
	s_addc_u32 s21, s19, 0
	s_cmp_eq_u32 s58, 12
	s_cselect_b32 s23, s9, s21
	s_cselect_b32 s22, s55, s20
	s_cselect_b32 s21, s13, s57
	s_cselect_b32 s20, s12, s56
	v_lshl_add_u64 v[162:163], s[18:19], 0, v[160:161]
	s_add_i32 m0, s29, 0xc000
	ds_read_b128 v[192:195], v188
	ds_read_b128 v[196:199], v188 offset:1024
	ds_read_b128 v[200:203], v188 offset:2048
	ds_read_b128 v[204:207], v188 offset:3072
	ds_read_b128 v[208:211], v188 offset:4096
	ds_read_b128 v[212:215], v188 offset:5120
	ds_read_b128 v[216:219], v188 offset:6144
	ds_read_b128 v[220:223], v188 offset:7168
	global_load_lds_dwordx4 v[162:163], off
	v_lshl_add_u64 v[162:163], s[18:19], 0, v[158:159]
	s_add_i32 m0, s29, 0xe000
	s_nop 0
	global_load_lds_dwordx4 v[162:163], off
	s_waitcnt lgkmcnt(8)
	s_barrier
	s_waitcnt lgkmcnt(0)
	s_setprio 1
	s_waitcnt lgkmcnt(0)
	v_mfma_scale_f32_16x16x128_f8f6f4 v[140:143], v[0:7], v[192:199], v[140:143], v189, v190 op_sel_hi:[0,0,0]
	v_mfma_scale_f32_16x16x128_f8f6f4 v[136:139], v[8:15], v[192:199], v[136:139], v189, v190 op_sel_hi:[0,0,0]
	v_mfma_scale_f32_16x16x128_f8f6f4 v[132:135], v[0:7], v[200:207], v[132:135], v189, v190 op_sel_hi:[0,0,0]
	v_mfma_scale_f32_16x16x128_f8f6f4 v[128:131], v[8:15], v[200:207], v[128:131], v189, v190 op_sel_hi:[0,0,0]
	v_mfma_scale_f32_16x16x128_f8f6f4 v[124:127], v[0:7], v[208:215], v[124:127], v189, v190 op_sel_hi:[0,0,0]
	v_mfma_scale_f32_16x16x128_f8f6f4 v[120:123], v[8:15], v[208:215], v[120:123], v189, v190 op_sel_hi:[0,0,0]
	v_mfma_scale_f32_16x16x128_f8f6f4 v[116:119], v[0:7], v[216:223], v[116:119], v189, v190 op_sel_hi:[0,0,0]
	v_mfma_scale_f32_16x16x128_f8f6f4 v[112:115], v[8:15], v[216:223], v[112:115], v189, v190 op_sel_hi:[0,0,0]
	s_setprio 0
	s_barrier
	s_mov_b32 m0, s30
	v_lshl_add_u64 v[162:163], s[20:21], 0, v[146:147]
	ds_read_b128 v[224:227], v171
	ds_read_b128 v[228:231], v178
	ds_read_b128 v[232:235], v179
	ds_read_b128 v[236:239], v180
	global_load_lds_dwordx4 v[162:163], off
	v_lshl_add_u64 v[164:165], s[20:21], 0, v[144:145]
	s_mov_b32 m0, s31
	s_nop 0
	global_load_lds_dwordx4 v[164:165], off
	s_barrier
	s_waitcnt lgkmcnt(0)
	s_setprio 1
	s_waitcnt lgkmcnt(0)
	v_mfma_scale_f32_16x16x128_f8f6f4 v[84:87], v[224:231], v[192:199], v[84:87], v189, v190 op_sel_hi:[0,0,0]
	v_mfma_scale_f32_16x16x128_f8f6f4 v[76:79], v[232:239], v[192:199], v[76:79], v189, v190 op_sel_hi:[0,0,0]
	v_mfma_scale_f32_16x16x128_f8f6f4 v[68:71], v[224:231], v[200:207], v[68:71], v189, v190 op_sel_hi:[0,0,0]
	v_mfma_scale_f32_16x16x128_f8f6f4 v[64:67], v[232:239], v[200:207], v[64:67], v189, v190 op_sel_hi:[0,0,0]
	v_mfma_scale_f32_16x16x128_f8f6f4 v[60:63], v[224:231], v[208:215], v[60:63], v189, v190 op_sel_hi:[0,0,0]
	v_mfma_scale_f32_16x16x128_f8f6f4 v[56:59], v[232:239], v[208:215], v[56:59], v189, v190 op_sel_hi:[0,0,0]
	v_mfma_scale_f32_16x16x128_f8f6f4 v[52:55], v[224:231], v[216:223], v[52:55], v189, v190 op_sel_hi:[0,0,0]
	v_mfma_scale_f32_16x16x128_f8f6f4 v[48:51], v[232:239], v[216:223], v[48:51], v189, v190 op_sel_hi:[0,0,0]
	s_setprio 0
	s_mov_b32 m0, s29
	v_lshl_add_u64 v[166:167], s[22:23], 0, v[148:149]
	s_barrier
	ds_read_b128 v[192:195], v188 offset:16384
	ds_read_b128 v[196:199], v188 offset:17408
	ds_read_b128 v[200:203], v188 offset:18432
	ds_read_b128 v[204:207], v188 offset:19456
	ds_read_b128 v[208:211], v188 offset:20480
	ds_read_b128 v[212:215], v188 offset:21504
	ds_read_b128 v[216:219], v188 offset:22528
	ds_read_b128 v[220:223], v188 offset:23552
	global_load_lds_dwordx4 v[166:167], off
	v_lshl_add_u64 v[168:169], s[22:23], 0, v[150:151]
	s_mov_b32 m0, s33
	s_nop 0
	global_load_lds_dwordx4 v[168:169], off
	s_barrier
	s_waitcnt lgkmcnt(0)
	s_setprio 1
	s_waitcnt lgkmcnt(0)
	v_mfma_scale_f32_16x16x128_f8f6f4 v[108:111], v[0:7], v[192:199], v[108:111], v189, v190 op_sel_hi:[0,0,0]
	v_mfma_scale_f32_16x16x128_f8f6f4 v[104:107], v[8:15], v[192:199], v[104:107], v189, v190 op_sel_hi:[0,0,0]
	v_mfma_scale_f32_16x16x128_f8f6f4 v[100:103], v[0:7], v[200:207], v[100:103], v189, v190 op_sel_hi:[0,0,0]
	v_mfma_scale_f32_16x16x128_f8f6f4 v[96:99], v[8:15], v[200:207], v[96:99], v189, v190 op_sel_hi:[0,0,0]
	v_mfma_scale_f32_16x16x128_f8f6f4 v[92:95], v[0:7], v[208:215], v[92:95], v189, v190 op_sel_hi:[0,0,0]
	v_mfma_scale_f32_16x16x128_f8f6f4 v[88:91], v[8:15], v[208:215], v[88:91], v189, v190 op_sel_hi:[0,0,0]
	v_mfma_scale_f32_16x16x128_f8f6f4 v[80:83], v[0:7], v[216:223], v[80:83], v189, v190 op_sel_hi:[0,0,0]
	v_mfma_scale_f32_16x16x128_f8f6f4 v[72:75], v[8:15], v[216:223], v[72:75], v189, v190 op_sel_hi:[0,0,0]
	s_setprio 0
	s_barrier
	s_add_u32 s60, s20, 0x40000
	s_addc_u32 s61, s21, 0
	s_mov_b32 m0, s34
	v_lshl_add_u64 v[0:1], s[60:61], 0, v[146:147]
	global_load_lds_dwordx4 v[0:1], off
	v_lshl_add_u64 v[0:1], s[60:61], 0, v[144:145]
	s_mov_b32 m0, s35
	s_nop 0
	global_load_lds_dwordx4 v[0:1], off
	s_waitcnt vmcnt(6)
	s_barrier
	s_setprio 1
	v_mfma_scale_f32_16x16x128_f8f6f4 v[44:47], v[224:231], v[192:199], v[44:47], v189, v190 op_sel_hi:[0,0,0]
	v_mfma_scale_f32_16x16x128_f8f6f4 v[40:43], v[232:239], v[192:199], v[40:43], v189, v190 op_sel_hi:[0,0,0]
	v_mfma_scale_f32_16x16x128_f8f6f4 v[36:39], v[224:231], v[200:207], v[36:39], v189, v190 op_sel_hi:[0,0,0]
	v_mfma_scale_f32_16x16x128_f8f6f4 v[32:35], v[232:239], v[200:207], v[32:35], v189, v190 op_sel_hi:[0,0,0]
	v_mfma_scale_f32_16x16x128_f8f6f4 v[28:31], v[224:231], v[208:215], v[28:31], v189, v190 op_sel_hi:[0,0,0]
	v_mfma_scale_f32_16x16x128_f8f6f4 v[24:27], v[232:239], v[208:215], v[24:27], v189, v190 op_sel_hi:[0,0,0]
	v_mfma_scale_f32_16x16x128_f8f6f4 v[20:23], v[224:231], v[216:223], v[20:23], v189, v190 op_sel_hi:[0,0,0]
	v_mfma_scale_f32_16x16x128_f8f6f4 v[16:19], v[232:239], v[216:223], v[16:19], v189, v190 op_sel_hi:[0,0,0]
	s_setprio 0
	s_barrier
	ds_read_b128 v[0:3], v172
	ds_read_b128 v[4:7], v181
	ds_read_b128 v[8:11], v182
	ds_read_b128 v[12:15], v183
	s_mov_b32 m0, s36
	v_lshl_add_u64 v[224:225], s[22:23], 0, v[152:153]
	ds_read_b128 v[192:195], v188 offset:32768
	ds_read_b128 v[196:199], v188 offset:33792
	ds_read_b128 v[200:203], v188 offset:34816
	ds_read_b128 v[204:207], v188 offset:35840
	ds_read_b128 v[208:211], v188 offset:36864
	ds_read_b128 v[212:215], v188 offset:37888
	ds_read_b128 v[216:219], v188 offset:38912
	ds_read_b128 v[220:223], v188 offset:39936
	global_load_lds_dwordx4 v[224:225], off
	v_lshl_add_u64 v[224:225], s[22:23], 0, v[154:155]
	s_mov_b32 m0, s37
	s_nop 0
	global_load_lds_dwordx4 v[224:225], off
	s_waitcnt lgkmcnt(8)
	s_barrier
	s_waitcnt lgkmcnt(0)
	s_setprio 1
	s_waitcnt lgkmcnt(0)
	v_mfma_scale_f32_16x16x128_f8f6f4 v[140:143], v[0:7], v[192:199], v[140:143], v189, v190 op_sel_hi:[0,0,0]
	v_mfma_scale_f32_16x16x128_f8f6f4 v[136:139], v[8:15], v[192:199], v[136:139], v189, v190 op_sel_hi:[0,0,0]
	v_mfma_scale_f32_16x16x128_f8f6f4 v[132:135], v[0:7], v[200:207], v[132:135], v189, v190 op_sel_hi:[0,0,0]
	v_mfma_scale_f32_16x16x128_f8f6f4 v[128:131], v[8:15], v[200:207], v[128:131], v189, v190 op_sel_hi:[0,0,0]
	v_mfma_scale_f32_16x16x128_f8f6f4 v[124:127], v[0:7], v[208:215], v[124:127], v189, v190 op_sel_hi:[0,0,0]
	v_mfma_scale_f32_16x16x128_f8f6f4 v[120:123], v[8:15], v[208:215], v[120:123], v189, v190 op_sel_hi:[0,0,0]
	v_mfma_scale_f32_16x16x128_f8f6f4 v[116:119], v[0:7], v[216:223], v[116:119], v189, v190 op_sel_hi:[0,0,0]
	v_mfma_scale_f32_16x16x128_f8f6f4 v[112:115], v[8:15], v[216:223], v[112:115], v189, v190 op_sel_hi:[0,0,0]
	s_setprio 0
	s_barrier
	s_mov_b32 m0, s40
	v_lshl_add_u64 v[162:163], v[162:163], 0, s[4:5]
	ds_read_b128 v[224:227], v173
	ds_read_b128 v[228:231], v184
	ds_read_b128 v[232:235], v185
	ds_read_b128 v[236:239], v186
	global_load_lds_dwordx4 v[162:163], off
	v_lshl_add_u64 v[162:163], v[164:165], 0, s[4:5]
	s_mov_b32 m0, s41
	s_nop 0
	global_load_lds_dwordx4 v[162:163], off
	s_barrier
	s_waitcnt lgkmcnt(0)
	s_setprio 1
	s_waitcnt lgkmcnt(0)
	v_mfma_scale_f32_16x16x128_f8f6f4 v[84:87], v[224:231], v[192:199], v[84:87], v189, v190 op_sel_hi:[0,0,0]
	v_mfma_scale_f32_16x16x128_f8f6f4 v[76:79], v[232:239], v[192:199], v[76:79], v189, v190 op_sel_hi:[0,0,0]
	v_mfma_scale_f32_16x16x128_f8f6f4 v[68:71], v[224:231], v[200:207], v[68:71], v189, v190 op_sel_hi:[0,0,0]
	v_mfma_scale_f32_16x16x128_f8f6f4 v[64:67], v[232:239], v[200:207], v[64:67], v189, v190 op_sel_hi:[0,0,0]
	v_mfma_scale_f32_16x16x128_f8f6f4 v[60:63], v[224:231], v[208:215], v[60:63], v189, v190 op_sel_hi:[0,0,0]
	v_mfma_scale_f32_16x16x128_f8f6f4 v[56:59], v[232:239], v[208:215], v[56:59], v189, v190 op_sel_hi:[0,0,0]
	v_mfma_scale_f32_16x16x128_f8f6f4 v[52:55], v[224:231], v[216:223], v[52:55], v189, v190 op_sel_hi:[0,0,0]
	v_mfma_scale_f32_16x16x128_f8f6f4 v[48:51], v[232:239], v[216:223], v[48:51], v189, v190 op_sel_hi:[0,0,0]
	s_setprio 0
	s_mov_b32 m0, s42
	v_lshl_add_u64 v[162:163], v[166:167], 0, s[4:5]
	s_barrier
	ds_read_b128 v[192:195], v188 offset:49152
	ds_read_b128 v[196:199], v188 offset:50176
	ds_read_b128 v[200:203], v188 offset:51200
	ds_read_b128 v[204:207], v188 offset:52224
	ds_read_b128 v[208:211], v188 offset:53248
	ds_read_b128 v[212:215], v188 offset:54272
	ds_read_b128 v[216:219], v188 offset:55296
	ds_read_b128 v[220:223], v188 offset:56320
	global_load_lds_dwordx4 v[162:163], off
	v_lshl_add_u64 v[162:163], v[168:169], 0, s[4:5]
	s_mov_b32 m0, s43
	s_nop 0
	global_load_lds_dwordx4 v[162:163], off
	s_barrier
	s_waitcnt lgkmcnt(0)
	s_setprio 1
	s_waitcnt lgkmcnt(0)
	v_mfma_scale_f32_16x16x128_f8f6f4 v[108:111], v[0:7], v[192:199], v[108:111], v189, v190 op_sel_hi:[0,0,0]
	v_mfma_scale_f32_16x16x128_f8f6f4 v[104:107], v[8:15], v[192:199], v[104:107], v189, v190 op_sel_hi:[0,0,0]
	v_mfma_scale_f32_16x16x128_f8f6f4 v[100:103], v[0:7], v[200:207], v[100:103], v189, v190 op_sel_hi:[0,0,0]
	v_mfma_scale_f32_16x16x128_f8f6f4 v[96:99], v[8:15], v[200:207], v[96:99], v189, v190 op_sel_hi:[0,0,0]
	v_mfma_scale_f32_16x16x128_f8f6f4 v[92:95], v[0:7], v[208:215], v[92:95], v189, v190 op_sel_hi:[0,0,0]
	v_mfma_scale_f32_16x16x128_f8f6f4 v[88:91], v[8:15], v[208:215], v[88:91], v189, v190 op_sel_hi:[0,0,0]
	v_mfma_scale_f32_16x16x128_f8f6f4 v[80:83], v[0:7], v[216:223], v[80:83], v189, v190 op_sel_hi:[0,0,0]
	v_mfma_scale_f32_16x16x128_f8f6f4 v[72:75], v[8:15], v[216:223], v[72:75], v189, v190 op_sel_hi:[0,0,0]
	s_setprio 0
	s_barrier
	s_add_u32 s20, s20, 0x40080
	s_addc_u32 s21, s21, 0
	s_mov_b32 m0, s44
	v_lshl_add_u64 v[0:1], s[20:21], 0, v[146:147]
	global_load_lds_dwordx4 v[0:1], off
	v_lshl_add_u64 v[0:1], s[20:21], 0, v[144:145]
	s_mov_b32 m0, s45
	s_nop 0
	global_load_lds_dwordx4 v[0:1], off
	s_waitcnt vmcnt(6)
	s_barrier
	s_setprio 1
	v_mfma_scale_f32_16x16x128_f8f6f4 v[44:47], v[224:231], v[192:199], v[44:47], v189, v190 op_sel_hi:[0,0,0]
	v_mfma_scale_f32_16x16x128_f8f6f4 v[40:43], v[232:239], v[192:199], v[40:43], v189, v190 op_sel_hi:[0,0,0]
	v_mfma_scale_f32_16x16x128_f8f6f4 v[36:39], v[224:231], v[200:207], v[36:39], v189, v190 op_sel_hi:[0,0,0]
	v_mfma_scale_f32_16x16x128_f8f6f4 v[32:35], v[232:239], v[200:207], v[32:35], v189, v190 op_sel_hi:[0,0,0]
	v_mfma_scale_f32_16x16x128_f8f6f4 v[28:31], v[224:231], v[208:215], v[28:31], v189, v190 op_sel_hi:[0,0,0]
	v_mfma_scale_f32_16x16x128_f8f6f4 v[24:27], v[232:239], v[208:215], v[24:27], v189, v190 op_sel_hi:[0,0,0]
	v_mfma_scale_f32_16x16x128_f8f6f4 v[20:23], v[224:231], v[216:223], v[20:23], v189, v190 op_sel_hi:[0,0,0]
	v_mfma_scale_f32_16x16x128_f8f6f4 v[16:19], v[232:239], v[216:223], v[16:19], v189, v190 op_sel_hi:[0,0,0]
	s_setprio 0
	s_add_i32 s58, s58, 2
	s_add_u32 s18, s18, 0x100
	s_addc_u32 s19, s19, 0
	s_add_u32 s56, s56, 0x100
	s_addc_u32 s57, s57, 0
	s_cmp_gt_u32 s58, 13
	s_barrier
	s_cbranch_scc0 .LBB0_1419
	s_nop 15
	s_nop 15
	v_lshl_or_b32 v8, s54, 8, v187
	s_ashr_i32 s17, s16, 31
	s_lshl_b64 s[16:17], s[16:17], 19
	v_lshl_add_u64 v[10:11], v[156:157], 0, s[16:17]
	v_ashrrev_i32_e32 v9, 31, v8
	v_lshl_add_u64 v[8:9], v[10:11], 0, v[8:9]
	v_mbcnt_lo_u32_b32 v10, -1, 0
	v_mbcnt_hi_u32_b32 v10, -1, v10
	v_and_b32_e32 v10, 16, v10
	v_mov_b32_e32 v12, 0x8000
	v_cmp_eq_u32_e32 vcc, 0, v10
	s_nop 1
	v_cndmask_b32_e32 v12, -8, v12, vcc
	v_ashrrev_i32_e32 v13, 31, v12
	v_lshl_add_u64 v[8:9], v[8:9], 0, v[12:13]
	v_med3_f32 v132, v132, s7, v191
	v_med3_f32 v133, v133, s7, v191
	v_med3_f32 v134, v134, s7, v191
	v_med3_f32 v135, v135, s7, v191
	v_med3_f32 v128, v128, s7, v191
	v_med3_f32 v129, v129, s7, v191
	v_med3_f32 v130, v130, s7, v191
	v_med3_f32 v131, v131, s7, v191
	v_cvt_pk_fp8_f32 v224, v132, v133
	v_cvt_pk_fp8_f32 v225, v128, v129
	v_cvt_pk_fp8_f32 v224, v134, v135 op_sel:[0,0,1]
	v_cvt_pk_fp8_f32 v225, v130, v131 op_sel:[0,0,1]
	v_med3_f32 v140, v140, s7, v191
	v_med3_f32 v141, v141, s7, v191
	v_med3_f32 v142, v142, s7, v191
	v_med3_f32 v143, v143, s7, v191
	v_med3_f32 v136, v136, s7, v191
	v_med3_f32 v137, v137, s7, v191
	v_med3_f32 v138, v138, s7, v191
	v_med3_f32 v139, v139, s7, v191
	v_cvt_pk_fp8_f32 v226, v140, v141
	v_cvt_pk_fp8_f32 v227, v136, v137
	v_cvt_pk_fp8_f32 v226, v142, v143 op_sel:[0,0,1]
	v_cvt_pk_fp8_f32 v227, v138, v139 op_sel:[0,0,1]
	s_nop 1
	v_permlane16_swap_b32_e32 v224, v226
	v_permlane16_swap_b32_e32 v225, v227
	global_store_dwordx4 v[8:9], v[224:227], off
	v_med3_f32 v68, v68, s7, v191
	v_med3_f32 v69, v69, s7, v191
	v_med3_f32 v70, v70, s7, v191
	v_med3_f32 v71, v71, s7, v191
	v_med3_f32 v64, v64, s7, v191
	v_med3_f32 v65, v65, s7, v191
	v_med3_f32 v66, v66, s7, v191
	v_med3_f32 v67, v67, s7, v191
	v_cvt_pk_fp8_f32 v228, v68, v69
	v_cvt_pk_fp8_f32 v229, v64, v65
	v_cvt_pk_fp8_f32 v228, v70, v71 op_sel:[0,0,1]
	v_cvt_pk_fp8_f32 v229, v66, v67 op_sel:[0,0,1]
	v_med3_f32 v84, v84, s7, v191
	v_med3_f32 v85, v85, s7, v191
	v_med3_f32 v86, v86, s7, v191
	v_med3_f32 v87, v87, s7, v191
	v_med3_f32 v76, v76, s7, v191
	v_med3_f32 v77, v77, s7, v191
	v_med3_f32 v78, v78, s7, v191
	v_med3_f32 v79, v79, s7, v191
	v_cvt_pk_fp8_f32 v230, v84, v85
	v_cvt_pk_fp8_f32 v231, v76, v77
	v_cvt_pk_fp8_f32 v230, v86, v87 op_sel:[0,0,1]
	v_cvt_pk_fp8_f32 v231, v78, v79 op_sel:[0,0,1]
	s_nop 1
	v_permlane16_swap_b32_e32 v228, v230
	v_permlane16_swap_b32_e32 v229, v231
	global_store_dwordx4 v[8:9], v[228:231], off offset:128
	v_lshl_add_u64 v[8:9], v[8:9], 0, s[62:63]
	v_med3_f32 v116, v116, s7, v191
	v_med3_f32 v117, v117, s7, v191
	v_med3_f32 v118, v118, s7, v191
	v_med3_f32 v119, v119, s7, v191
	v_med3_f32 v112, v112, s7, v191
	v_med3_f32 v113, v113, s7, v191
	v_med3_f32 v114, v114, s7, v191
	v_med3_f32 v115, v115, s7, v191
	v_cvt_pk_fp8_f32 v232, v116, v117
	v_cvt_pk_fp8_f32 v233, v112, v113
	v_cvt_pk_fp8_f32 v232, v118, v119 op_sel:[0,0,1]
	v_cvt_pk_fp8_f32 v233, v114, v115 op_sel:[0,0,1]
	v_med3_f32 v124, v124, s7, v191
	v_med3_f32 v125, v125, s7, v191
	v_med3_f32 v126, v126, s7, v191
	v_med3_f32 v127, v127, s7, v191
	v_med3_f32 v120, v120, s7, v191
	v_med3_f32 v121, v121, s7, v191
	v_med3_f32 v122, v122, s7, v191
	v_med3_f32 v123, v123, s7, v191
	v_cvt_pk_fp8_f32 v234, v124, v125
	v_cvt_pk_fp8_f32 v235, v120, v121
	v_cvt_pk_fp8_f32 v234, v126, v127 op_sel:[0,0,1]
	v_cvt_pk_fp8_f32 v235, v122, v123 op_sel:[0,0,1]
	s_nop 1
	v_permlane16_swap_b32_e32 v232, v234
	v_permlane16_swap_b32_e32 v233, v235
	global_store_dwordx4 v[8:9], v[232:235], off
	v_med3_f32 v52, v52, s7, v191
	v_med3_f32 v53, v53, s7, v191
	v_med3_f32 v54, v54, s7, v191
	v_med3_f32 v55, v55, s7, v191
	v_med3_f32 v48, v48, s7, v191
	v_med3_f32 v49, v49, s7, v191
	v_med3_f32 v50, v50, s7, v191
	v_med3_f32 v51, v51, s7, v191
	v_cvt_pk_fp8_f32 v236, v52, v53
	v_cvt_pk_fp8_f32 v237, v48, v49
	v_cvt_pk_fp8_f32 v236, v54, v55 op_sel:[0,0,1]
	v_cvt_pk_fp8_f32 v237, v50, v51 op_sel:[0,0,1]
	v_med3_f32 v60, v60, s7, v191
	v_med3_f32 v61, v61, s7, v191
	v_med3_f32 v62, v62, s7, v191
	v_med3_f32 v63, v63, s7, v191
	v_med3_f32 v56, v56, s7, v191
	v_med3_f32 v57, v57, s7, v191
	v_med3_f32 v58, v58, s7, v191
	v_med3_f32 v59, v59, s7, v191
	v_cvt_pk_fp8_f32 v238, v60, v61
	v_cvt_pk_fp8_f32 v239, v56, v57
	v_cvt_pk_fp8_f32 v238, v62, v63 op_sel:[0,0,1]
	v_cvt_pk_fp8_f32 v239, v58, v59 op_sel:[0,0,1]
	s_nop 1
	v_permlane16_swap_b32_e32 v236, v238
	v_permlane16_swap_b32_e32 v237, v239
	global_store_dwordx4 v[8:9], v[236:239], off offset:128
	v_lshl_add_u64 v[8:9], v[8:9], 0, s[64:65]
	v_med3_f32 v100, v100, s7, v191
	v_med3_f32 v101, v101, s7, v191
	v_med3_f32 v102, v102, s7, v191
	v_med3_f32 v103, v103, s7, v191
	v_med3_f32 v96, v96, s7, v191
	v_med3_f32 v97, v97, s7, v191
	v_med3_f32 v98, v98, s7, v191
	v_med3_f32 v99, v99, s7, v191
	v_cvt_pk_fp8_f32 v224, v100, v101
	v_cvt_pk_fp8_f32 v225, v96, v97
	v_cvt_pk_fp8_f32 v224, v102, v103 op_sel:[0,0,1]
	v_cvt_pk_fp8_f32 v225, v98, v99 op_sel:[0,0,1]
	v_med3_f32 v108, v108, s7, v191
	v_med3_f32 v109, v109, s7, v191
	v_med3_f32 v110, v110, s7, v191
	v_med3_f32 v111, v111, s7, v191
	v_med3_f32 v104, v104, s7, v191
	v_med3_f32 v105, v105, s7, v191
	v_med3_f32 v106, v106, s7, v191
	v_med3_f32 v107, v107, s7, v191
	v_cvt_pk_fp8_f32 v226, v108, v109
	v_cvt_pk_fp8_f32 v227, v104, v105
	v_cvt_pk_fp8_f32 v226, v110, v111 op_sel:[0,0,1]
	v_cvt_pk_fp8_f32 v227, v106, v107 op_sel:[0,0,1]
	s_nop 1
	v_permlane16_swap_b32_e32 v224, v226
	v_permlane16_swap_b32_e32 v225, v227
	global_store_dwordx4 v[8:9], v[224:227], off
	v_med3_f32 v36, v36, s7, v191
	v_med3_f32 v37, v37, s7, v191
	v_med3_f32 v38, v38, s7, v191
	v_med3_f32 v39, v39, s7, v191
	v_med3_f32 v32, v32, s7, v191
	v_med3_f32 v33, v33, s7, v191
	v_med3_f32 v34, v34, s7, v191
	v_med3_f32 v35, v35, s7, v191
	v_cvt_pk_fp8_f32 v228, v36, v37
	v_cvt_pk_fp8_f32 v229, v32, v33
	v_cvt_pk_fp8_f32 v228, v38, v39 op_sel:[0,0,1]
	v_cvt_pk_fp8_f32 v229, v34, v35 op_sel:[0,0,1]
	v_med3_f32 v44, v44, s7, v191
	v_med3_f32 v45, v45, s7, v191
	v_med3_f32 v46, v46, s7, v191
	v_med3_f32 v47, v47, s7, v191
	v_med3_f32 v40, v40, s7, v191
	v_med3_f32 v41, v41, s7, v191
	v_med3_f32 v42, v42, s7, v191
	v_med3_f32 v43, v43, s7, v191
	v_cvt_pk_fp8_f32 v230, v44, v45
	v_cvt_pk_fp8_f32 v231, v40, v41
	v_cvt_pk_fp8_f32 v230, v46, v47 op_sel:[0,0,1]
	v_cvt_pk_fp8_f32 v231, v42, v43 op_sel:[0,0,1]
	s_nop 1
	v_permlane16_swap_b32_e32 v228, v230
	v_permlane16_swap_b32_e32 v229, v231
	global_store_dwordx4 v[8:9], v[228:231], off offset:128
	v_lshl_add_u64 v[8:9], v[8:9], 0, s[62:63]
	v_med3_f32 v80, v80, s7, v191
	v_med3_f32 v81, v81, s7, v191
	v_med3_f32 v82, v82, s7, v191
	v_med3_f32 v83, v83, s7, v191
	v_med3_f32 v72, v72, s7, v191
	v_med3_f32 v73, v73, s7, v191
	v_med3_f32 v74, v74, s7, v191
	v_med3_f32 v75, v75, s7, v191
	v_cvt_pk_fp8_f32 v232, v80, v81
	v_cvt_pk_fp8_f32 v233, v72, v73
	v_cvt_pk_fp8_f32 v232, v82, v83 op_sel:[0,0,1]
	v_cvt_pk_fp8_f32 v233, v74, v75 op_sel:[0,0,1]
	v_med3_f32 v92, v92, s7, v191
	v_med3_f32 v93, v93, s7, v191
	v_med3_f32 v94, v94, s7, v191
	v_med3_f32 v95, v95, s7, v191
	v_med3_f32 v88, v88, s7, v191
	v_med3_f32 v89, v89, s7, v191
	v_med3_f32 v90, v90, s7, v191
	v_med3_f32 v91, v91, s7, v191
	v_cvt_pk_fp8_f32 v234, v92, v93
	v_cvt_pk_fp8_f32 v235, v88, v89
	v_cvt_pk_fp8_f32 v234, v94, v95 op_sel:[0,0,1]
	v_cvt_pk_fp8_f32 v235, v90, v91 op_sel:[0,0,1]
	s_nop 1
	v_permlane16_swap_b32_e32 v232, v234
	v_permlane16_swap_b32_e32 v233, v235
	global_store_dwordx4 v[8:9], v[232:235], off
	v_med3_f32 v20, v20, s7, v191
	v_med3_f32 v21, v21, s7, v191
	v_med3_f32 v22, v22, s7, v191
	v_med3_f32 v23, v23, s7, v191
	v_med3_f32 v16, v16, s7, v191
	v_med3_f32 v17, v17, s7, v191
	v_med3_f32 v18, v18, s7, v191
	v_med3_f32 v19, v19, s7, v191
	v_cvt_pk_fp8_f32 v236, v20, v21
	v_cvt_pk_fp8_f32 v237, v16, v17
	v_cvt_pk_fp8_f32 v236, v22, v23 op_sel:[0,0,1]
	v_cvt_pk_fp8_f32 v237, v18, v19 op_sel:[0,0,1]
	v_med3_f32 v28, v28, s7, v191
	v_med3_f32 v29, v29, s7, v191
	v_med3_f32 v30, v30, s7, v191
	v_med3_f32 v31, v31, s7, v191
	v_med3_f32 v24, v24, s7, v191
	v_med3_f32 v25, v25, s7, v191
	v_med3_f32 v26, v26, s7, v191
	v_med3_f32 v27, v27, s7, v191
	v_cvt_pk_fp8_f32 v238, v28, v29
	v_cvt_pk_fp8_f32 v239, v24, v25
	v_cvt_pk_fp8_f32 v238, v30, v31 op_sel:[0,0,1]
	v_cvt_pk_fp8_f32 v239, v26, v27 op_sel:[0,0,1]
	s_nop 1
	v_permlane16_swap_b32_e32 v236, v238
	v_permlane16_swap_b32_e32 v237, v239
	global_store_dwordx4 v[8:9], v[236:239], off offset:128
	s_and_b64 vcc, exec, s[10:11]
	s_mov_b32 s17, s53
	s_mov_b32 s54, s52
	s_mov_b32 s16, s8
	s_mov_b64 s[20:21], s[12:13]
	s_mov_b64 s[18:19], s[14:15]
	s_cbranch_vccz .LBB0_1413
	s_waitcnt vmcnt(0)
	s_cmpk_gt_u32 s24, 0xff
	s_cbranch_scc1 .LBB0_1423
	s_barrier
